# baseline (speedup 1.0000x reference)
.Lou_loop:
	s_waitcnt lgkmcnt(0)
	v_mfma_f32_16x16x32_bf16 v[64:67], v[176:179], v[160:163], v[64:67]
	ds_read_b128 v[200:203], v11 offset:0
	v_mfma_f32_16x16x32_bf16 v[68:71], v[176:179], v[164:167], v[68:71]
	ds_read_b128 v[204:207], v11 offset:2048
	v_mfma_f32_16x16x32_bf16 v[72:75], v[176:179], v[168:171], v[72:75]
	ds_read_b128 v[208:211], v11 offset:4096
	v_mfma_f32_16x16x32_bf16 v[76:79], v[176:179], v[172:175], v[76:79]
	ds_read_b128 v[212:215], v11 offset:6144
	v_mfma_f32_16x16x32_bf16 v[80:83], v[180:183], v[160:163], v[80:83]
	ds_read_b128 v[216:219], v13 offset:0
	v_mfma_f32_16x16x32_bf16 v[84:87], v[180:183], v[164:167], v[84:87]
	ds_read_b128 v[220:223], v13 offset:2048
	v_mfma_f32_16x16x32_bf16 v[88:91], v[180:183], v[168:171], v[88:91]
	ds_read_b128 v[224:227], v13 offset:4096
	v_mfma_f32_16x16x32_bf16 v[92:95], v[180:183], v[172:175], v[92:95]
	ds_read_b128 v[228:231], v13 offset:6144
	v_mfma_f32_16x16x32_bf16 v[96:99], v[184:187], v[160:163], v[96:99]
	ds_read_b128 v[232:235], v13 offset:8192
	v_mfma_f32_16x16x32_bf16 v[100:103], v[184:187], v[164:167], v[100:103]
	ds_read_b128 v[236:239], v13 offset:10240
	v_mfma_f32_16x16x32_bf16 v[104:107], v[184:187], v[168:171], v[104:107]
	s_add_u32 m0, s20, 0x5000
	v_mfma_f32_16x16x32_bf16 v[108:111], v[184:187], v[172:175], v[108:111]
	global_load_lds_dwordx4 v3, s[18:19]
	v_mfma_f32_16x16x32_bf16 v[112:115], v[188:191], v[160:163], v[112:115]
	s_add_u32 m0, s20, 0x6000
	v_mfma_f32_16x16x32_bf16 v[116:119], v[188:191], v[164:167], v[116:119]
	global_load_lds_dwordx4 v4, s[18:19]
	v_mfma_f32_16x16x32_bf16 v[120:123], v[188:191], v[168:171], v[120:123]
	s_add_u32 m0, s20, 0x7000
	v_mfma_f32_16x16x32_bf16 v[124:127], v[188:191], v[172:175], v[124:127]
	global_load_lds_dwordx4 v5, s[18:19]
	v_mfma_f32_16x16x32_bf16 v[128:131], v[192:195], v[160:163], v[128:131]
	s_add_u32 m0, s20, 0x8000
	v_mfma_f32_16x16x32_bf16 v[132:135], v[192:195], v[164:167], v[132:135]
	global_load_lds_dwordx4 v6, s[18:19]
	v_mfma_f32_16x16x32_bf16 v[136:139], v[192:195], v[168:171], v[136:139]
	s_add_u32 m0, s20, 0x9000
	v_mfma_f32_16x16x32_bf16 v[140:143], v[192:195], v[172:175], v[140:143]
	global_load_lds_dwordx4 v7, s[18:19]
	v_mfma_f32_16x16x32_bf16 v[144:147], v[196:199], v[160:163], v[144:147]
	s_add_u32 s16, s16, 0x80
	s_addc_u32 s17, s17, 0
	s_add_u32 s18, s18, 0x80
	s_addc_u32 s19, s19, 0
	v_mfma_f32_16x16x32_bf16 v[148:151], v[196:199], v[164:167], v[148:151]
	s_add_u32 s20, s20, 0xa000
	s_sub_u32 s22, s20, 0x28000
	s_cmp_ge_u32 s20, 0x28000
	s_cselect_b32 s20, s22, s20
	v_mfma_f32_16x16x32_bf16 v[152:155], v[196:199], v[168:171], v[152:155]
	v_add_u32_e32 v10, s21, v8
	v_add_u32_e32 v12, s21, v9
	v_xor_b32_e32 v11, 64, v10
	v_xor_b32_e32 v13, 64, v12
	v_mfma_f32_16x16x32_bf16 v[156:159], v[196:199], v[172:175], v[156:159]
	s_add_u32 s21, s21, 0xa000
	s_sub_u32 s23, s21, 0x28000
	s_cmp_ge_u32 s21, 0x28000
	s_cselect_b32 s21, s23, s21
	s_waitcnt lgkmcnt(0)
	v_mfma_f32_16x16x32_bf16 v[64:67], v[216:219], v[200:203], v[64:67]
	v_mfma_f32_16x16x32_bf16 v[68:71], v[216:219], v[204:207], v[68:71]
	v_mfma_f32_16x16x32_bf16 v[72:75], v[216:219], v[208:211], v[72:75]
	v_mfma_f32_16x16x32_bf16 v[76:79], v[216:219], v[212:215], v[76:79]
	s_waitcnt vmcnt(20)
	s_barrier
	v_mfma_f32_16x16x32_bf16 v[80:83], v[220:223], v[200:203], v[80:83]
	ds_read_b128 v[160:163], v10 offset:0
	v_mfma_f32_16x16x32_bf16 v[84:87], v[220:223], v[204:207], v[84:87]
	ds_read_b128 v[164:167], v10 offset:2048
	v_mfma_f32_16x16x32_bf16 v[88:91], v[220:223], v[208:211], v[88:91]
	ds_read_b128 v[168:171], v10 offset:4096
	v_mfma_f32_16x16x32_bf16 v[92:95], v[220:223], v[212:215], v[92:95]
	ds_read_b128 v[172:175], v10 offset:6144
	v_mfma_f32_16x16x32_bf16 v[96:99], v[224:227], v[200:203], v[96:99]
	ds_read_b128 v[176:179], v12 offset:0
	v_mfma_f32_16x16x32_bf16 v[100:103], v[224:227], v[204:207], v[100:103]
	ds_read_b128 v[180:183], v12 offset:2048
	v_mfma_f32_16x16x32_bf16 v[104:107], v[224:227], v[208:211], v[104:107]
	ds_read_b128 v[184:187], v12 offset:4096
	v_mfma_f32_16x16x32_bf16 v[108:111], v[224:227], v[212:215], v[108:111]
	ds_read_b128 v[188:191], v12 offset:6144
	v_mfma_f32_16x16x32_bf16 v[112:115], v[228:231], v[200:203], v[112:115]
	ds_read_b128 v[192:195], v12 offset:8192
	v_mfma_f32_16x16x32_bf16 v[116:119], v[228:231], v[204:207], v[116:119]
	ds_read_b128 v[196:199], v12 offset:10240
	v_mfma_f32_16x16x32_bf16 v[120:123], v[228:231], v[208:211], v[120:123]
	s_add_u32 m0, s20, 0x0
	v_mfma_f32_16x16x32_bf16 v[124:127], v[228:231], v[212:215], v[124:127]
	global_load_lds_dwordx4 v2, s[16:17]
	v_mfma_f32_16x16x32_bf16 v[128:131], v[232:235], v[200:203], v[128:131]
	s_add_u32 m0, s20, 0x1000
	v_mfma_f32_16x16x32_bf16 v[132:135], v[232:235], v[204:207], v[132:135]
	global_load_lds_dwordx4 v3, s[16:17]
	v_mfma_f32_16x16x32_bf16 v[136:139], v[232:235], v[208:211], v[136:139]
	s_add_u32 m0, s20, 0x2000
	v_mfma_f32_16x16x32_bf16 v[140:143], v[232:235], v[212:215], v[140:143]
	global_load_lds_dwordx4 v4, s[16:17]
	v_mfma_f32_16x16x32_bf16 v[144:147], v[236:239], v[200:203], v[144:147]
	s_add_u32 m0, s20, 0x3000
	v_mfma_f32_16x16x32_bf16 v[148:151], v[236:239], v[204:207], v[148:151]
	global_load_lds_dwordx4 v5, s[16:17]
	v_mfma_f32_16x16x32_bf16 v[152:155], v[236:239], v[208:211], v[152:155]
	s_add_u32 m0, s20, 0x4000
	v_mfma_f32_16x16x32_bf16 v[156:159], v[236:239], v[212:215], v[156:159]
	global_load_lds_dwordx4 v2, s[18:19]
	s_add_u32 s15, s15, 1
	s_cmp_lt_u32 s15, 8
	s_cbranch_scc1 .Lou_loop
	s_waitcnt lgkmcnt(0)
	v_mfma_f32_16x16x32_bf16 v[64:67], v[176:179], v[160:163], v[64:67]
	ds_read_b128 v[200:203], v11 offset:0
	v_mfma_f32_16x16x32_bf16 v[68:71], v[176:179], v[164:167], v[68:71]
	ds_read_b128 v[204:207], v11 offset:2048
	v_mfma_f32_16x16x32_bf16 v[72:75], v[176:179], v[168:171], v[72:75]
	ds_read_b128 v[208:211], v11 offset:4096
	v_mfma_f32_16x16x32_bf16 v[76:79], v[176:179], v[172:175], v[76:79]
	ds_read_b128 v[212:215], v11 offset:6144
	v_mfma_f32_16x16x32_bf16 v[80:83], v[180:183], v[160:163], v[80:83]
	ds_read_b128 v[216:219], v13 offset:0
	v_mfma_f32_16x16x32_bf16 v[84:87], v[180:183], v[164:167], v[84:87]
	ds_read_b128 v[220:223], v13 offset:2048
	v_mfma_f32_16x16x32_bf16 v[88:91], v[180:183], v[168:171], v[88:91]
	ds_read_b128 v[224:227], v13 offset:4096
	v_mfma_f32_16x16x32_bf16 v[92:95], v[180:183], v[172:175], v[92:95]
	ds_read_b128 v[228:231], v13 offset:6144
	v_mfma_f32_16x16x32_bf16 v[96:99], v[184:187], v[160:163], v[96:99]
	ds_read_b128 v[232:235], v13 offset:8192
	v_mfma_f32_16x16x32_bf16 v[100:103], v[184:187], v[164:167], v[100:103]
	ds_read_b128 v[236:239], v13 offset:10240
	v_mfma_f32_16x16x32_bf16 v[104:107], v[184:187], v[168:171], v[104:107]
	s_add_u32 m0, s20, 0x5000
	v_mfma_f32_16x16x32_bf16 v[108:111], v[184:187], v[172:175], v[108:111]
	global_load_lds_dwordx4 v3, s[18:19]
	v_mfma_f32_16x16x32_bf16 v[112:115], v[188:191], v[160:163], v[112:115]
	s_add_u32 m0, s20, 0x6000
	v_mfma_f32_16x16x32_bf16 v[116:119], v[188:191], v[164:167], v[116:119]
	global_load_lds_dwordx4 v4, s[18:19]
	v_mfma_f32_16x16x32_bf16 v[120:123], v[188:191], v[168:171], v[120:123]
	s_add_u32 m0, s20, 0x7000
	v_mfma_f32_16x16x32_bf16 v[124:127], v[188:191], v[172:175], v[124:127]
	global_load_lds_dwordx4 v5, s[18:19]
	v_mfma_f32_16x16x32_bf16 v[128:131], v[192:195], v[160:163], v[128:131]
	s_add_u32 m0, s20, 0x8000
	v_mfma_f32_16x16x32_bf16 v[132:135], v[192:195], v[164:167], v[132:135]
	global_load_lds_dwordx4 v6, s[18:19]
	v_mfma_f32_16x16x32_bf16 v[136:139], v[192:195], v[168:171], v[136:139]
	s_add_u32 m0, s20, 0x9000
	v_mfma_f32_16x16x32_bf16 v[140:143], v[192:195], v[172:175], v[140:143]
	global_load_lds_dwordx4 v7, s[18:19]
	v_mfma_f32_16x16x32_bf16 v[144:147], v[196:199], v[160:163], v[144:147]
	s_add_u32 s16, s16, 0x80
	s_addc_u32 s17, s17, 0
	s_add_u32 s18, s18, 0x80
	s_addc_u32 s19, s19, 0
	v_mfma_f32_16x16x32_bf16 v[148:151], v[196:199], v[164:167], v[148:151]
	s_add_u32 s20, s20, 0xa000
	s_sub_u32 s22, s20, 0x28000
	s_cmp_ge_u32 s20, 0x28000
	s_cselect_b32 s20, s22, s20
	v_mfma_f32_16x16x32_bf16 v[152:155], v[196:199], v[168:171], v[152:155]
	v_add_u32_e32 v10, s21, v8
	v_add_u32_e32 v12, s21, v9
	v_xor_b32_e32 v11, 64, v10
	v_xor_b32_e32 v13, 64, v12
	v_mfma_f32_16x16x32_bf16 v[156:159], v[196:199], v[172:175], v[156:159]
	s_add_u32 s21, s21, 0xa000
	s_sub_u32 s23, s21, 0x28000
	s_cmp_ge_u32 s21, 0x28000
	s_cselect_b32 s21, s23, s21
	s_waitcnt lgkmcnt(0)
	v_mfma_f32_16x16x32_bf16 v[64:67], v[216:219], v[200:203], v[64:67]
	v_mfma_f32_16x16x32_bf16 v[68:71], v[216:219], v[204:207], v[68:71]
	v_mfma_f32_16x16x32_bf16 v[72:75], v[216:219], v[208:211], v[72:75]
	v_mfma_f32_16x16x32_bf16 v[76:79], v[216:219], v[212:215], v[76:79]
	s_waitcnt vmcnt(20)
	s_barrier
	v_mfma_f32_16x16x32_bf16 v[80:83], v[220:223], v[200:203], v[80:83]
	ds_read_b128 v[160:163], v10 offset:0
	v_mfma_f32_16x16x32_bf16 v[84:87], v[220:223], v[204:207], v[84:87]
	ds_read_b128 v[164:167], v10 offset:2048
	v_mfma_f32_16x16x32_bf16 v[88:91], v[220:223], v[208:211], v[88:91]
	ds_read_b128 v[168:171], v10 offset:4096
	v_mfma_f32_16x16x32_bf16 v[92:95], v[220:223], v[212:215], v[92:95]
	ds_read_b128 v[172:175], v10 offset:6144
	v_mfma_f32_16x16x32_bf16 v[96:99], v[224:227], v[200:203], v[96:99]
	ds_read_b128 v[176:179], v12 offset:0
	v_mfma_f32_16x16x32_bf16 v[100:103], v[224:227], v[204:207], v[100:103]
	ds_read_b128 v[180:183], v12 offset:2048
	v_mfma_f32_16x16x32_bf16 v[104:107], v[224:227], v[208:211], v[104:107]
	ds_read_b128 v[184:187], v12 offset:4096
	v_mfma_f32_16x16x32_bf16 v[108:111], v[224:227], v[212:215], v[108:111]
	ds_read_b128 v[188:191], v12 offset:6144
	v_mfma_f32_16x16x32_bf16 v[112:115], v[228:231], v[200:203], v[112:115]
	ds_read_b128 v[192:195], v12 offset:8192
	v_mfma_f32_16x16x32_bf16 v[116:119], v[228:231], v[204:207], v[116:119]
	ds_read_b128 v[196:199], v12 offset:10240
	v_mfma_f32_16x16x32_bf16 v[120:123], v[228:231], v[208:211], v[120:123]
	global_load_dwordx4 v[240:243], v60, s[24:25]
	v_mfma_f32_16x16x32_bf16 v[124:127], v[228:231], v[212:215], v[124:127]
	global_load_dwordx4 v[244:247], v60, s[24:25] offset:64
	v_mfma_f32_16x16x32_bf16 v[128:131], v[232:235], v[200:203], v[128:131]
	global_load_dwordx4 v[248:251], v60, s[24:25] offset:128
	v_mfma_f32_16x16x32_bf16 v[132:135], v[232:235], v[204:207], v[132:135]
	global_load_dwordx4 v[252:255], v60, s[24:25] offset:192
	v_mfma_f32_16x16x32_bf16 v[136:139], v[232:235], v[208:211], v[136:139]
	global_load_dwordx4 v[48:51], v60, s[24:25] offset:256
	v_mfma_f32_16x16x32_bf16 v[140:143], v[232:235], v[212:215], v[140:143]
	global_load_dwordx4 v[52:55], v60, s[24:25] offset:320
	v_mfma_f32_16x16x32_bf16 v[144:147], v[236:239], v[200:203], v[144:147]
	global_load_dwordx4 v[16:19], v56, s[8:9] offset:0
	v_mfma_f32_16x16x32_bf16 v[148:151], v[236:239], v[204:207], v[148:151]
	global_load_dwordx4 v[20:23], v56, s[8:9] offset:64
	v_mfma_f32_16x16x32_bf16 v[152:155], v[236:239], v[208:211], v[152:155]
	global_load_dwordx4 v[24:27], v56, s[8:9] offset:128
	v_mfma_f32_16x16x32_bf16 v[156:159], v[236:239], v[212:215], v[156:159]
	global_load_dwordx4 v[28:31], v56, s[8:9] offset:192
	global_load_dwordx4 v[32:35], v56, s[8:9] offset:256
	global_load_dwordx4 v[36:39], v56, s[8:9] offset:320
	global_load_dwordx4 v[40:43], v57, s[8:9] offset:0
	global_load_dwordx4 v[44:47], v57, s[8:9] offset:64
	s_waitcnt lgkmcnt(0)
	v_mfma_f32_16x16x32_bf16 v[64:67], v[176:179], v[160:163], v[64:67]
	ds_read_b128 v[200:203], v11 offset:0
	v_mfma_f32_16x16x32_bf16 v[68:71], v[176:179], v[164:167], v[68:71]
	ds_read_b128 v[204:207], v11 offset:2048
	v_mfma_f32_16x16x32_bf16 v[72:75], v[176:179], v[168:171], v[72:75]
	ds_read_b128 v[208:211], v11 offset:4096
	v_mfma_f32_16x16x32_bf16 v[76:79], v[176:179], v[172:175], v[76:79]
	ds_read_b128 v[212:215], v11 offset:6144
	v_mfma_f32_16x16x32_bf16 v[80:83], v[180:183], v[160:163], v[80:83]
	ds_read_b128 v[216:219], v13 offset:0
	v_mfma_f32_16x16x32_bf16 v[84:87], v[180:183], v[164:167], v[84:87]
	ds_read_b128 v[220:223], v13 offset:2048
	v_mfma_f32_16x16x32_bf16 v[88:91], v[180:183], v[168:171], v[88:91]
	ds_read_b128 v[224:227], v13 offset:4096
	v_mfma_f32_16x16x32_bf16 v[92:95], v[180:183], v[172:175], v[92:95]
	ds_read_b128 v[228:231], v13 offset:6144
	v_mfma_f32_16x16x32_bf16 v[96:99], v[184:187], v[160:163], v[96:99]
	ds_read_b128 v[232:235], v13 offset:8192
	v_mfma_f32_16x16x32_bf16 v[100:103], v[184:187], v[164:167], v[100:103]
	ds_read_b128 v[236:239], v13 offset:10240
	v_mfma_f32_16x16x32_bf16 v[104:107], v[184:187], v[168:171], v[104:107]
	v_mfma_f32_16x16x32_bf16 v[108:111], v[184:187], v[172:175], v[108:111]
	v_mfma_f32_16x16x32_bf16 v[112:115], v[188:191], v[160:163], v[112:115]
	v_mfma_f32_16x16x32_bf16 v[116:119], v[188:191], v[164:167], v[116:119]
	v_mfma_f32_16x16x32_bf16 v[120:123], v[188:191], v[168:171], v[120:123]
	v_mfma_f32_16x16x32_bf16 v[124:127], v[188:191], v[172:175], v[124:127]
	v_mfma_f32_16x16x32_bf16 v[128:131], v[192:195], v[160:163], v[128:131]
	v_mfma_f32_16x16x32_bf16 v[132:135], v[192:195], v[164:167], v[132:135]
	v_mfma_f32_16x16x32_bf16 v[136:139], v[192:195], v[168:171], v[136:139]
	v_mfma_f32_16x16x32_bf16 v[140:143], v[192:195], v[172:175], v[140:143]
	v_mfma_f32_16x16x32_bf16 v[144:147], v[196:199], v[160:163], v[144:147]
	v_add_u32_e32 v10, s21, v8
	v_add_u32_e32 v12, s21, v9
	v_xor_b32_e32 v11, 64, v10
	v_xor_b32_e32 v13, 64, v12
	v_mfma_f32_16x16x32_bf16 v[148:151], v[196:199], v[164:167], v[148:151]
	s_add_u32 s21, s21, 0xa000
	s_sub_u32 s23, s21, 0x28000
	s_cmp_ge_u32 s21, 0x28000
	s_cselect_b32 s21, s23, s21
	v_mfma_f32_16x16x32_bf16 v[152:155], v[196:199], v[168:171], v[152:155]
	v_mfma_f32_16x16x32_bf16 v[156:159], v[196:199], v[172:175], v[156:159]
	s_waitcnt lgkmcnt(0)
	v_mfma_f32_16x16x32_bf16 v[64:67], v[216:219], v[200:203], v[64:67]
	v_mfma_f32_16x16x32_bf16 v[68:71], v[216:219], v[204:207], v[68:71]
	v_mfma_f32_16x16x32_bf16 v[72:75], v[216:219], v[208:211], v[72:75]
	v_mfma_f32_16x16x32_bf16 v[76:79], v[216:219], v[212:215], v[76:79]
	s_waitcnt vmcnt(24)
	s_barrier
	v_mfma_f32_16x16x32_bf16 v[80:83], v[220:223], v[200:203], v[80:83]
	ds_read_b128 v[160:163], v10 offset:0
	v_mfma_f32_16x16x32_bf16 v[84:87], v[220:223], v[204:207], v[84:87]
	ds_read_b128 v[164:167], v10 offset:2048
	v_mfma_f32_16x16x32_bf16 v[88:91], v[220:223], v[208:211], v[88:91]
	ds_read_b128 v[168:171], v10 offset:4096
	v_mfma_f32_16x16x32_bf16 v[92:95], v[220:223], v[212:215], v[92:95]
	ds_read_b128 v[172:175], v10 offset:6144
	v_mfma_f32_16x16x32_bf16 v[96:99], v[224:227], v[200:203], v[96:99]
	ds_read_b128 v[176:179], v12 offset:0
	v_mfma_f32_16x16x32_bf16 v[100:103], v[224:227], v[204:207], v[100:103]
	ds_read_b128 v[180:183], v12 offset:2048
	v_mfma_f32_16x16x32_bf16 v[104:107], v[224:227], v[208:211], v[104:107]
	ds_read_b128 v[184:187], v12 offset:4096
	v_mfma_f32_16x16x32_bf16 v[108:111], v[224:227], v[212:215], v[108:111]
	ds_read_b128 v[188:191], v12 offset:6144
	v_mfma_f32_16x16x32_bf16 v[112:115], v[228:231], v[200:203], v[112:115]
	ds_read_b128 v[192:195], v12 offset:8192
	v_mfma_f32_16x16x32_bf16 v[116:119], v[228:231], v[204:207], v[116:119]
	ds_read_b128 v[196:199], v12 offset:10240
	v_mfma_f32_16x16x32_bf16 v[120:123], v[228:231], v[208:211], v[120:123]
	v_mfma_f32_16x16x32_bf16 v[124:127], v[228:231], v[212:215], v[124:127]
	v_mfma_f32_16x16x32_bf16 v[128:131], v[232:235], v[200:203], v[128:131]
	v_mfma_f32_16x16x32_bf16 v[132:135], v[232:235], v[204:207], v[132:135]
	v_mfma_f32_16x16x32_bf16 v[136:139], v[232:235], v[208:211], v[136:139]
	v_mfma_f32_16x16x32_bf16 v[140:143], v[232:235], v[212:215], v[140:143]
	v_mfma_f32_16x16x32_bf16 v[144:147], v[236:239], v[200:203], v[144:147]
	v_mfma_f32_16x16x32_bf16 v[148:151], v[236:239], v[204:207], v[148:151]
	v_mfma_f32_16x16x32_bf16 v[152:155], v[236:239], v[208:211], v[152:155]
	v_mfma_f32_16x16x32_bf16 v[156:159], v[236:239], v[212:215], v[156:159]
	s_waitcnt lgkmcnt(0)
	v_mfma_f32_16x16x32_bf16 v[64:67], v[176:179], v[160:163], v[64:67]
	ds_read_b128 v[200:203], v11 offset:0
	v_mfma_f32_16x16x32_bf16 v[68:71], v[176:179], v[164:167], v[68:71]
	ds_read_b128 v[204:207], v11 offset:2048
	v_mfma_f32_16x16x32_bf16 v[72:75], v[176:179], v[168:171], v[72:75]
	ds_read_b128 v[208:211], v11 offset:4096
	v_mfma_f32_16x16x32_bf16 v[76:79], v[176:179], v[172:175], v[76:79]
	ds_read_b128 v[212:215], v11 offset:6144
	v_mfma_f32_16x16x32_bf16 v[80:83], v[180:183], v[160:163], v[80:83]
	ds_read_b128 v[216:219], v13 offset:0
	v_mfma_f32_16x16x32_bf16 v[84:87], v[180:183], v[164:167], v[84:87]
	ds_read_b128 v[220:223], v13 offset:2048
	v_mfma_f32_16x16x32_bf16 v[88:91], v[180:183], v[168:171], v[88:91]
	ds_read_b128 v[224:227], v13 offset:4096
	v_mfma_f32_16x16x32_bf16 v[92:95], v[180:183], v[172:175], v[92:95]
	ds_read_b128 v[228:231], v13 offset:6144
	v_mfma_f32_16x16x32_bf16 v[96:99], v[184:187], v[160:163], v[96:99]
	ds_read_b128 v[232:235], v13 offset:8192
	v_mfma_f32_16x16x32_bf16 v[100:103], v[184:187], v[164:167], v[100:103]
	ds_read_b128 v[236:239], v13 offset:10240
	v_mfma_f32_16x16x32_bf16 v[104:107], v[184:187], v[168:171], v[104:107]
	v_mfma_f32_16x16x32_bf16 v[108:111], v[184:187], v[172:175], v[108:111]
	v_mfma_f32_16x16x32_bf16 v[112:115], v[188:191], v[160:163], v[112:115]
	v_mfma_f32_16x16x32_bf16 v[116:119], v[188:191], v[164:167], v[116:119]
	v_mfma_f32_16x16x32_bf16 v[120:123], v[188:191], v[168:171], v[120:123]
	v_mfma_f32_16x16x32_bf16 v[124:127], v[188:191], v[172:175], v[124:127]
	v_mfma_f32_16x16x32_bf16 v[128:131], v[192:195], v[160:163], v[128:131]
	v_mfma_f32_16x16x32_bf16 v[132:135], v[192:195], v[164:167], v[132:135]
	v_mfma_f32_16x16x32_bf16 v[136:139], v[192:195], v[168:171], v[136:139]
	v_mfma_f32_16x16x32_bf16 v[140:143], v[192:195], v[172:175], v[140:143]
	v_mfma_f32_16x16x32_bf16 v[144:147], v[196:199], v[160:163], v[144:147]
	v_add_u32_e32 v10, s21, v8
	v_add_u32_e32 v12, s21, v9
	v_xor_b32_e32 v11, 64, v10
	v_xor_b32_e32 v13, 64, v12
	v_mfma_f32_16x16x32_bf16 v[148:151], v[196:199], v[164:167], v[148:151]
	s_add_u32 s21, s21, 0xa000
	s_sub_u32 s23, s21, 0x28000
	s_cmp_ge_u32 s21, 0x28000
	s_cselect_b32 s21, s23, s21
	v_mfma_f32_16x16x32_bf16 v[152:155], v[196:199], v[168:171], v[152:155]
	v_mfma_f32_16x16x32_bf16 v[156:159], v[196:199], v[172:175], v[156:159]
	s_waitcnt lgkmcnt(0)
	v_mfma_f32_16x16x32_bf16 v[64:67], v[216:219], v[200:203], v[64:67]
	v_mfma_f32_16x16x32_bf16 v[68:71], v[216:219], v[204:207], v[68:71]
	v_mfma_f32_16x16x32_bf16 v[72:75], v[216:219], v[208:211], v[72:75]
	v_mfma_f32_16x16x32_bf16 v[76:79], v[216:219], v[212:215], v[76:79]
	s_waitcnt vmcnt(14)
	s_barrier
	v_mfma_f32_16x16x32_bf16 v[80:83], v[220:223], v[200:203], v[80:83]
	ds_read_b128 v[160:163], v10 offset:0
	v_mfma_f32_16x16x32_bf16 v[84:87], v[220:223], v[204:207], v[84:87]
	ds_read_b128 v[164:167], v10 offset:2048
	v_mfma_f32_16x16x32_bf16 v[88:91], v[220:223], v[208:211], v[88:91]
	ds_read_b128 v[168:171], v10 offset:4096
	v_mfma_f32_16x16x32_bf16 v[92:95], v[220:223], v[212:215], v[92:95]
	ds_read_b128 v[172:175], v10 offset:6144
	v_mfma_f32_16x16x32_bf16 v[96:99], v[224:227], v[200:203], v[96:99]
	ds_read_b128 v[176:179], v12 offset:0
	v_mfma_f32_16x16x32_bf16 v[100:103], v[224:227], v[204:207], v[100:103]
	ds_read_b128 v[180:183], v12 offset:2048
	v_mfma_f32_16x16x32_bf16 v[104:107], v[224:227], v[208:211], v[104:107]
	ds_read_b128 v[184:187], v12 offset:4096
	v_mfma_f32_16x16x32_bf16 v[108:111], v[224:227], v[212:215], v[108:111]
	ds_read_b128 v[188:191], v12 offset:6144
	v_mfma_f32_16x16x32_bf16 v[112:115], v[228:231], v[200:203], v[112:115]
	ds_read_b128 v[192:195], v12 offset:8192
	v_mfma_f32_16x16x32_bf16 v[116:119], v[228:231], v[204:207], v[116:119]
	ds_read_b128 v[196:199], v12 offset:10240
	v_mfma_f32_16x16x32_bf16 v[120:123], v[228:231], v[208:211], v[120:123]
	v_mfma_f32_16x16x32_bf16 v[124:127], v[228:231], v[212:215], v[124:127]
	v_mfma_f32_16x16x32_bf16 v[128:131], v[232:235], v[200:203], v[128:131]
	v_mfma_f32_16x16x32_bf16 v[132:135], v[232:235], v[204:207], v[132:135]
	v_mfma_f32_16x16x32_bf16 v[136:139], v[232:235], v[208:211], v[136:139]
	v_mfma_f32_16x16x32_bf16 v[140:143], v[232:235], v[212:215], v[140:143]
	v_mfma_f32_16x16x32_bf16 v[144:147], v[236:239], v[200:203], v[144:147]
	v_mfma_f32_16x16x32_bf16 v[148:151], v[236:239], v[204:207], v[148:151]
	v_mfma_f32_16x16x32_bf16 v[152:155], v[236:239], v[208:211], v[152:155]
	v_mfma_f32_16x16x32_bf16 v[156:159], v[236:239], v[212:215], v[156:159]
	s_waitcnt lgkmcnt(0)
	v_mfma_f32_16x16x32_bf16 v[64:67], v[176:179], v[160:163], v[64:67]
	ds_read_b128 v[200:203], v11 offset:0
	v_mfma_f32_16x16x32_bf16 v[68:71], v[176:179], v[164:167], v[68:71]
	ds_read_b128 v[204:207], v11 offset:2048
	v_mfma_f32_16x16x32_bf16 v[72:75], v[176:179], v[168:171], v[72:75]
	ds_read_b128 v[208:211], v11 offset:4096
	v_mfma_f32_16x16x32_bf16 v[76:79], v[176:179], v[172:175], v[76:79]
	ds_read_b128 v[212:215], v11 offset:6144
	v_mfma_f32_16x16x32_bf16 v[80:83], v[180:183], v[160:163], v[80:83]
	ds_read_b128 v[216:219], v13 offset:0
	v_mfma_f32_16x16x32_bf16 v[84:87], v[180:183], v[164:167], v[84:87]
	ds_read_b128 v[220:223], v13 offset:2048
	v_mfma_f32_16x16x32_bf16 v[88:91], v[180:183], v[168:171], v[88:91]
	ds_read_b128 v[224:227], v13 offset:4096
	v_mfma_f32_16x16x32_bf16 v[92:95], v[180:183], v[172:175], v[92:95]
	ds_read_b128 v[228:231], v13 offset:6144
	v_mfma_f32_16x16x32_bf16 v[96:99], v[184:187], v[160:163], v[96:99]
	ds_read_b128 v[232:235], v13 offset:8192
	v_mfma_f32_16x16x32_bf16 v[100:103], v[184:187], v[164:167], v[100:103]
	ds_read_b128 v[236:239], v13 offset:10240
	v_mfma_f32_16x16x32_bf16 v[104:107], v[184:187], v[168:171], v[104:107]
	v_mfma_f32_16x16x32_bf16 v[108:111], v[184:187], v[172:175], v[108:111]
	v_mfma_f32_16x16x32_bf16 v[112:115], v[188:191], v[160:163], v[112:115]
	v_mfma_f32_16x16x32_bf16 v[116:119], v[188:191], v[164:167], v[116:119]
	v_mfma_f32_16x16x32_bf16 v[120:123], v[188:191], v[168:171], v[120:123]
	v_mfma_f32_16x16x32_bf16 v[124:127], v[188:191], v[172:175], v[124:127]
	v_mfma_f32_16x16x32_bf16 v[128:131], v[192:195], v[160:163], v[128:131]
	v_mfma_f32_16x16x32_bf16 v[132:135], v[192:195], v[164:167], v[132:135]
	v_mfma_f32_16x16x32_bf16 v[136:139], v[192:195], v[168:171], v[136:139]
	v_mfma_f32_16x16x32_bf16 v[140:143], v[192:195], v[172:175], v[140:143]
	v_mfma_f32_16x16x32_bf16 v[144:147], v[196:199], v[160:163], v[144:147]
	v_mfma_f32_16x16x32_bf16 v[148:151], v[196:199], v[164:167], v[148:151]
	v_mfma_f32_16x16x32_bf16 v[152:155], v[196:199], v[168:171], v[152:155]
	v_mfma_f32_16x16x32_bf16 v[156:159], v[196:199], v[172:175], v[156:159]
	s_waitcnt lgkmcnt(0)
	v_mfma_f32_16x16x32_bf16 v[64:67], v[216:219], v[200:203], v[64:67]
	v_mfma_f32_16x16x32_bf16 v[68:71], v[216:219], v[204:207], v[68:71]
	global_load_dwordx4 v[160:163], v57, s[8:9] offset:128
	v_mfma_f32_16x16x32_bf16 v[72:75], v[216:219], v[208:211], v[72:75]
	v_mfma_f32_16x16x32_bf16 v[76:79], v[216:219], v[212:215], v[76:79]
	global_load_dwordx4 v[164:167], v57, s[8:9] offset:192
	v_mfma_f32_16x16x32_bf16 v[80:83], v[220:223], v[200:203], v[80:83]
	v_mfma_f32_16x16x32_bf16 v[84:87], v[220:223], v[204:207], v[84:87]
	global_load_dwordx4 v[168:171], v57, s[8:9] offset:256
	v_mfma_f32_16x16x32_bf16 v[88:91], v[220:223], v[208:211], v[88:91]
	v_mfma_f32_16x16x32_bf16 v[92:95], v[220:223], v[212:215], v[92:95]
	global_load_dwordx4 v[172:175], v57, s[8:9] offset:320
	v_mfma_f32_16x16x32_bf16 v[96:99], v[224:227], v[200:203], v[96:99]
	v_mfma_f32_16x16x32_bf16 v[100:103], v[224:227], v[204:207], v[100:103]
	global_load_dwordx4 v[176:179], v58, s[8:9] offset:0
	v_mfma_f32_16x16x32_bf16 v[104:107], v[224:227], v[208:211], v[104:107]
	v_mfma_f32_16x16x32_bf16 v[108:111], v[224:227], v[212:215], v[108:111]
	global_load_dwordx4 v[180:183], v58, s[8:9] offset:64
	v_mfma_f32_16x16x32_bf16 v[112:115], v[228:231], v[200:203], v[112:115]
	v_mfma_f32_16x16x32_bf16 v[116:119], v[228:231], v[204:207], v[116:119]
	global_load_dwordx4 v[184:187], v58, s[8:9] offset:128
	v_mfma_f32_16x16x32_bf16 v[120:123], v[228:231], v[208:211], v[120:123]
	v_mfma_f32_16x16x32_bf16 v[124:127], v[228:231], v[212:215], v[124:127]
	global_load_dwordx4 v[188:191], v58, s[8:9] offset:192
	v_mfma_f32_16x16x32_bf16 v[128:131], v[232:235], v[200:203], v[128:131]
	v_mfma_f32_16x16x32_bf16 v[132:135], v[232:235], v[204:207], v[132:135]
	global_load_dwordx4 v[192:195], v58, s[8:9] offset:256
	v_mfma_f32_16x16x32_bf16 v[136:139], v[232:235], v[208:211], v[136:139]
	v_mfma_f32_16x16x32_bf16 v[140:143], v[232:235], v[212:215], v[140:143]
	global_load_dwordx4 v[196:199], v58, s[8:9] offset:320
	v_mfma_f32_16x16x32_bf16 v[144:147], v[236:239], v[200:203], v[144:147]
	v_mfma_f32_16x16x32_bf16 v[148:151], v[236:239], v[204:207], v[148:151]
	v_mfma_f32_16x16x32_bf16 v[152:155], v[236:239], v[208:211], v[152:155]
	v_mfma_f32_16x16x32_bf16 v[156:159], v[236:239], v[212:215], v[156:159]
	v_and_b32_e32 v12, 63, v0
	v_cmp_gt_u32_e32 vcc, 16, v12
	v_xor_b32_e32 v13, 16, v12
	v_lshlrev_b32_e32 v13, 2, v13
	v_xor_b32_e32 v12, 32, v12
	v_lshlrev_b32_e32 v12, 2, v12
	v_bfe_u32 v14, v0, 6, 1
	v_mul_u32_u24_e32 v14, 0x60, v14
	v_bfe_u32 v15, v0, 4, 2
	v_lshl_add_u32 v14, v15, 2, v14
	v_add_u32_e32 v14, s13, v14
	v_lshlrev_b32_e32 v14, 2, v14
	global_load_dwordx4 v[200:203], v59, s[8:9] offset:0
	global_load_dwordx4 v[204:207], v59, s[8:9] offset:64
	global_load_dwordx4 v[208:211], v59, s[8:9] offset:128
	global_load_dwordx4 v[212:215], v59, s[8:9] offset:192
	global_load_dwordx4 v[216:219], v59, s[8:9] offset:256
	global_load_dwordx4 v[220:223], v59, s[8:9] offset:320
	v_lshrrev_b32_e32 v60, 1, v56
	v_lshrrev_b32_e32 v61, 1, v57
	v_lshrrev_b32_e32 v62, 1, v58
	v_lshrrev_b32_e32 v63, 1, v59
	v_bfe_u32 v2, v0, 4, 1
	v_mul_u32_u24_e32 v2, 24, v2
	v_add_u32_e32 v60, v60, v2
	v_add_u32_e32 v61, v61, v2
	v_add_u32_e32 v62, v62, v2
	v_add_u32_e32 v63, v63, v2
	v_bfe_u32 v8, v0, 7, 1
	v_and_b32_e32 v9, 15, v0
	v_lshl_add_u32 v8, v8, 6, v9
	v_add_u32_e32 v8, s12, v8
	v_lshlrev_b32_e32 v8, 6, v8
	v_bfe_u32 v9, v0, 6, 1
	v_lshlrev_b32_e32 v9, 1, v9
	v_add_u32_e32 v9, s30, v9
	v_lshl_add_u32 v8, v9, 2, v8
	v_add_u32_e32 v9, 0x400, v8
	v_add_u32_e32 v10, 0x400, v9
	v_add_u32_e32 v11, 0x400, v10
	s_waitcnt vmcnt(23)
	v_pk_add_f32 v[64:65], v[64:65], v[16:17]
	v_pk_add_f32 v[66:67], v[66:67], v[18:19]
	global_store_dwordx4 v56, v[64:67], s[10:11]
	v_pk_mul_f32 v[224:225], v[240:241], v[64:65]
	v_pk_mul_f32 v[226:227], v[242:243], v[66:67]
	v_cvt_pk_bf16_f32 v4, v224, v225
	v_cvt_pk_bf16_f32 v5, v226, v227
	v_pk_mul_f32 v[230:231], v[64:65], v[64:65]
	v_pk_mul_f32 v[232:233], v[66:67], v[66:67]
	v_add_f32_e32 v230, v230, v231
	v_add_f32_e32 v230, v232, v230
	v_add_f32_e32 v234, v233, v230
	s_waitcnt vmcnt(23)
	v_pk_add_f32 v[80:81], v[80:81], v[20:21]
	v_pk_add_f32 v[82:83], v[82:83], v[22:23]
	global_store_dwordx4 v56, v[80:83], s[10:11] offset:64
	v_pk_mul_f32 v[224:225], v[244:245], v[80:81]
	v_pk_mul_f32 v[226:227], v[246:247], v[82:83]
	v_cvt_pk_bf16_f32 v6, v224, v225
	v_cvt_pk_bf16_f32 v7, v226, v227
	s_nop 1
	v_permlane16_swap_b32 v4, v6
	v_permlane16_swap_b32 v5, v7
	global_store_dwordx4 v60, v[4:7], s[28:29]
	v_pk_mul_f32 v[230:231], v[80:81], v[80:81]
	v_pk_mul_f32 v[232:233], v[82:83], v[82:83]
	v_add_f32_e32 v230, v230, v231
	v_add_f32_e32 v230, v232, v230
	v_add_f32_e32 v230, v233, v230
	v_add_f32_e32 v234, v234, v230
	s_waitcnt vmcnt(24)
	v_pk_add_f32 v[96:97], v[96:97], v[24:25]
	v_pk_add_f32 v[98:99], v[98:99], v[26:27]
	global_store_dwordx4 v56, v[96:99], s[10:11] offset:128
	v_pk_mul_f32 v[224:225], v[248:249], v[96:97]
	v_pk_mul_f32 v[226:227], v[250:251], v[98:99]
	v_cvt_pk_bf16_f32 v4, v224, v225
	v_cvt_pk_bf16_f32 v5, v226, v227
	v_pk_mul_f32 v[230:231], v[96:97], v[96:97]
	v_pk_mul_f32 v[232:233], v[98:99], v[98:99]
	v_add_f32_e32 v230, v230, v231
	v_add_f32_e32 v230, v232, v230
	v_add_f32_e32 v230, v233, v230
	v_add_f32_e32 v234, v234, v230
	s_waitcnt vmcnt(24)
	v_pk_add_f32 v[112:113], v[112:113], v[28:29]
	v_pk_add_f32 v[114:115], v[114:115], v[30:31]
	global_store_dwordx4 v56, v[112:115], s[10:11] offset:192
	v_pk_mul_f32 v[224:225], v[252:253], v[112:113]
	v_pk_mul_f32 v[226:227], v[254:255], v[114:115]
	v_cvt_pk_bf16_f32 v6, v224, v225
	v_cvt_pk_bf16_f32 v7, v226, v227
	s_nop 1
	v_permlane16_swap_b32 v4, v6
	v_permlane16_swap_b32 v5, v7
	global_store_dwordx4 v60, v[4:7], s[28:29] offset:64
	v_pk_mul_f32 v[230:231], v[112:113], v[112:113]
	v_pk_mul_f32 v[232:233], v[114:115], v[114:115]
	v_add_f32_e32 v230, v230, v231
	v_add_f32_e32 v230, v232, v230
	v_add_f32_e32 v235, v233, v230
	s_waitcnt vmcnt(25)
	v_pk_add_f32 v[128:129], v[128:129], v[32:33]
	v_pk_add_f32 v[130:131], v[130:131], v[34:35]
	global_store_dwordx4 v56, v[128:131], s[10:11] offset:256
	v_pk_mul_f32 v[224:225], v[48:49], v[128:129]
	v_pk_mul_f32 v[226:227], v[50:51], v[130:131]
	v_cvt_pk_bf16_f32 v4, v224, v225
	v_cvt_pk_bf16_f32 v5, v226, v227
	v_pk_mul_f32 v[230:231], v[128:129], v[128:129]
	v_pk_mul_f32 v[232:233], v[130:131], v[130:131]
	v_add_f32_e32 v230, v230, v231
	v_add_f32_e32 v230, v232, v230
	v_add_f32_e32 v230, v233, v230
	v_add_f32_e32 v235, v235, v230
	s_waitcnt vmcnt(25)
	v_pk_add_f32 v[144:145], v[144:145], v[36:37]
	v_pk_add_f32 v[146:147], v[146:147], v[38:39]
	global_store_dwordx4 v56, v[144:147], s[10:11] offset:320
	v_pk_mul_f32 v[224:225], v[52:53], v[144:145]
	v_pk_mul_f32 v[226:227], v[54:55], v[146:147]
	v_cvt_pk_bf16_f32 v6, v224, v225
	v_cvt_pk_bf16_f32 v7, v226, v227
	s_nop 1
	v_permlane16_swap_b32 v4, v6
	v_permlane16_swap_b32 v5, v7
	global_store_dwordx4 v60, v[4:7], s[28:29] offset:128
	v_pk_mul_f32 v[230:231], v[144:145], v[144:145]
	v_pk_mul_f32 v[232:233], v[146:147], v[146:147]
	v_add_f32_e32 v230, v230, v231
	v_add_f32_e32 v230, v232, v230
	v_add_f32_e32 v230, v233, v230
	v_add_f32_e32 v235, v235, v230
	s_waitcnt vmcnt(26)
	v_pk_add_f32 v[68:69], v[68:69], v[40:41]
	v_pk_add_f32 v[70:71], v[70:71], v[42:43]
	global_store_dwordx4 v57, v[68:71], s[10:11]
	v_pk_mul_f32 v[224:225], v[240:241], v[68:69]
	v_pk_mul_f32 v[226:227], v[242:243], v[70:71]
	v_cvt_pk_bf16_f32 v4, v224, v225
	v_cvt_pk_bf16_f32 v5, v226, v227
	v_pk_mul_f32 v[230:231], v[68:69], v[68:69]
	v_pk_mul_f32 v[232:233], v[70:71], v[70:71]
	v_add_f32_e32 v230, v230, v231
	v_add_f32_e32 v230, v232, v230
	v_add_f32_e32 v236, v233, v230
	s_waitcnt vmcnt(26)
	v_pk_add_f32 v[84:85], v[84:85], v[44:45]
	v_pk_add_f32 v[86:87], v[86:87], v[46:47]
	global_store_dwordx4 v57, v[84:87], s[10:11] offset:64
	v_pk_mul_f32 v[224:225], v[244:245], v[84:85]
	v_pk_mul_f32 v[226:227], v[246:247], v[86:87]
	v_cvt_pk_bf16_f32 v6, v224, v225
	v_cvt_pk_bf16_f32 v7, v226, v227
	s_nop 1
	v_permlane16_swap_b32 v4, v6
	v_permlane16_swap_b32 v5, v7
	global_store_dwordx4 v61, v[4:7], s[28:29]
	v_pk_mul_f32 v[230:231], v[84:85], v[84:85]
	v_pk_mul_f32 v[232:233], v[86:87], v[86:87]
	v_add_f32_e32 v230, v230, v231
	v_add_f32_e32 v230, v232, v230
	v_add_f32_e32 v230, v233, v230
	v_add_f32_e32 v236, v236, v230
	s_waitcnt vmcnt(27)
	v_pk_add_f32 v[100:101], v[100:101], v[160:161]
	v_pk_add_f32 v[102:103], v[102:103], v[162:163]
	global_store_dwordx4 v57, v[100:103], s[10:11] offset:128
	v_pk_mul_f32 v[224:225], v[248:249], v[100:101]
	v_pk_mul_f32 v[226:227], v[250:251], v[102:103]
	v_cvt_pk_bf16_f32 v4, v224, v225
	v_cvt_pk_bf16_f32 v5, v226, v227
	v_pk_mul_f32 v[230:231], v[100:101], v[100:101]
	v_pk_mul_f32 v[232:233], v[102:103], v[102:103]
	v_add_f32_e32 v230, v230, v231
	v_add_f32_e32 v230, v232, v230
	v_add_f32_e32 v230, v233, v230
	v_add_f32_e32 v236, v236, v230
	s_waitcnt vmcnt(27)
	v_pk_add_f32 v[116:117], v[116:117], v[164:165]
	v_pk_add_f32 v[118:119], v[118:119], v[166:167]
	global_store_dwordx4 v57, v[116:119], s[10:11] offset:192
	v_pk_mul_f32 v[224:225], v[252:253], v[116:117]
	v_pk_mul_f32 v[226:227], v[254:255], v[118:119]
	v_cvt_pk_bf16_f32 v6, v224, v225
	v_cvt_pk_bf16_f32 v7, v226, v227
	s_nop 1
	v_permlane16_swap_b32 v4, v6
	v_permlane16_swap_b32 v5, v7
	global_store_dwordx4 v61, v[4:7], s[28:29] offset:64
	v_pk_mul_f32 v[230:231], v[116:117], v[116:117]
	v_pk_mul_f32 v[232:233], v[118:119], v[118:119]
	v_add_f32_e32 v230, v230, v231
	v_add_f32_e32 v230, v232, v230
	v_add_f32_e32 v237, v233, v230
	s_waitcnt vmcnt(28)
	v_pk_add_f32 v[132:133], v[132:133], v[168:169]
	v_pk_add_f32 v[134:135], v[134:135], v[170:171]
	global_store_dwordx4 v57, v[132:135], s[10:11] offset:256
	v_pk_mul_f32 v[224:225], v[48:49], v[132:133]
	v_pk_mul_f32 v[226:227], v[50:51], v[134:135]
	v_cvt_pk_bf16_f32 v4, v224, v225
	v_cvt_pk_bf16_f32 v5, v226, v227
	v_pk_mul_f32 v[230:231], v[132:133], v[132:133]
	v_pk_mul_f32 v[232:233], v[134:135], v[134:135]
	v_add_f32_e32 v230, v230, v231
	v_add_f32_e32 v230, v232, v230
	v_add_f32_e32 v230, v233, v230
	v_add_f32_e32 v237, v237, v230
	s_waitcnt vmcnt(28)
	v_pk_add_f32 v[148:149], v[148:149], v[172:173]
	v_pk_add_f32 v[150:151], v[150:151], v[174:175]
	global_store_dwordx4 v57, v[148:151], s[10:11] offset:320
	v_pk_mul_f32 v[224:225], v[52:53], v[148:149]
	v_pk_mul_f32 v[226:227], v[54:55], v[150:151]
	v_cvt_pk_bf16_f32 v6, v224, v225
	v_cvt_pk_bf16_f32 v7, v226, v227
	s_nop 1
	v_permlane16_swap_b32 v4, v6
	v_permlane16_swap_b32 v5, v7
	global_store_dwordx4 v61, v[4:7], s[28:29] offset:128
	v_pk_mul_f32 v[230:231], v[148:149], v[148:149]
	v_pk_mul_f32 v[232:233], v[150:151], v[150:151]
	v_add_f32_e32 v230, v230, v231
	v_add_f32_e32 v230, v232, v230
	v_add_f32_e32 v230, v233, v230
	v_add_f32_e32 v237, v237, v230
	s_waitcnt vmcnt(29)
	v_pk_add_f32 v[72:73], v[72:73], v[176:177]
	v_pk_add_f32 v[74:75], v[74:75], v[178:179]
	global_store_dwordx4 v58, v[72:75], s[10:11]
	v_pk_mul_f32 v[224:225], v[240:241], v[72:73]
	v_pk_mul_f32 v[226:227], v[242:243], v[74:75]
	v_cvt_pk_bf16_f32 v4, v224, v225
	v_cvt_pk_bf16_f32 v5, v226, v227
	v_pk_mul_f32 v[230:231], v[72:73], v[72:73]
	v_pk_mul_f32 v[232:233], v[74:75], v[74:75]
	v_add_f32_e32 v230, v230, v231
	v_add_f32_e32 v230, v232, v230
	v_add_f32_e32 v238, v233, v230
	s_waitcnt vmcnt(29)
	v_pk_add_f32 v[88:89], v[88:89], v[180:181]
	v_pk_add_f32 v[90:91], v[90:91], v[182:183]
	global_store_dwordx4 v58, v[88:91], s[10:11] offset:64
	v_pk_mul_f32 v[224:225], v[244:245], v[88:89]
	v_pk_mul_f32 v[226:227], v[246:247], v[90:91]
	v_cvt_pk_bf16_f32 v6, v224, v225
	v_cvt_pk_bf16_f32 v7, v226, v227
	s_nop 1
	v_permlane16_swap_b32 v4, v6
	v_permlane16_swap_b32 v5, v7
	global_store_dwordx4 v62, v[4:7], s[28:29]
	v_pk_mul_f32 v[230:231], v[88:89], v[88:89]
	v_pk_mul_f32 v[232:233], v[90:91], v[90:91]
	v_add_f32_e32 v230, v230, v231
	v_add_f32_e32 v230, v232, v230
	v_add_f32_e32 v230, v233, v230
	v_add_f32_e32 v238, v238, v230
	s_waitcnt vmcnt(30)
	v_pk_add_f32 v[104:105], v[104:105], v[184:185]
	v_pk_add_f32 v[106:107], v[106:107], v[186:187]
	global_store_dwordx4 v58, v[104:107], s[10:11] offset:128
	v_pk_mul_f32 v[224:225], v[248:249], v[104:105]
	v_pk_mul_f32 v[226:227], v[250:251], v[106:107]
	v_cvt_pk_bf16_f32 v4, v224, v225
	v_cvt_pk_bf16_f32 v5, v226, v227
	v_pk_mul_f32 v[230:231], v[104:105], v[104:105]
	v_pk_mul_f32 v[232:233], v[106:107], v[106:107]
	v_add_f32_e32 v230, v230, v231
	v_add_f32_e32 v230, v232, v230
	v_add_f32_e32 v230, v233, v230
	v_add_f32_e32 v238, v238, v230
	s_waitcnt vmcnt(30)
	v_pk_add_f32 v[120:121], v[120:121], v[188:189]
	v_pk_add_f32 v[122:123], v[122:123], v[190:191]
	global_store_dwordx4 v58, v[120:123], s[10:11] offset:192
	v_pk_mul_f32 v[224:225], v[252:253], v[120:121]
	v_pk_mul_f32 v[226:227], v[254:255], v[122:123]
	v_cvt_pk_bf16_f32 v6, v224, v225
	v_cvt_pk_bf16_f32 v7, v226, v227
	s_nop 1
	v_permlane16_swap_b32 v4, v6
	v_permlane16_swap_b32 v5, v7
	global_store_dwordx4 v62, v[4:7], s[28:29] offset:64
	v_pk_mul_f32 v[230:231], v[120:121], v[120:121]
	v_pk_mul_f32 v[232:233], v[122:123], v[122:123]
	v_add_f32_e32 v230, v230, v231
	v_add_f32_e32 v230, v232, v230
	v_add_f32_e32 v239, v233, v230
	s_waitcnt vmcnt(31)
	v_pk_add_f32 v[136:137], v[136:137], v[192:193]
	v_pk_add_f32 v[138:139], v[138:139], v[194:195]
	global_store_dwordx4 v58, v[136:139], s[10:11] offset:256
	v_pk_mul_f32 v[224:225], v[48:49], v[136:137]
	v_pk_mul_f32 v[226:227], v[50:51], v[138:139]
	v_cvt_pk_bf16_f32 v4, v224, v225
	v_cvt_pk_bf16_f32 v5, v226, v227
	v_pk_mul_f32 v[230:231], v[136:137], v[136:137]
	v_pk_mul_f32 v[232:233], v[138:139], v[138:139]
	v_add_f32_e32 v230, v230, v231
	v_add_f32_e32 v230, v232, v230
	v_add_f32_e32 v230, v233, v230
	v_add_f32_e32 v239, v239, v230
	s_waitcnt vmcnt(31)
	v_pk_add_f32 v[152:153], v[152:153], v[196:197]
	v_pk_add_f32 v[154:155], v[154:155], v[198:199]
	global_store_dwordx4 v58, v[152:155], s[10:11] offset:320
	v_pk_mul_f32 v[224:225], v[52:53], v[152:153]
	v_pk_mul_f32 v[226:227], v[54:55], v[154:155]
	v_cvt_pk_bf16_f32 v6, v224, v225
	v_cvt_pk_bf16_f32 v7, v226, v227
	s_nop 1
	v_permlane16_swap_b32 v4, v6
	v_permlane16_swap_b32 v5, v7
	global_store_dwordx4 v62, v[4:7], s[28:29] offset:128
	v_pk_mul_f32 v[230:231], v[152:153], v[152:153]
	v_pk_mul_f32 v[232:233], v[154:155], v[154:155]
	v_add_f32_e32 v230, v230, v231
	v_add_f32_e32 v230, v232, v230
	v_add_f32_e32 v230, v233, v230
	v_add_f32_e32 v239, v239, v230
	s_waitcnt vmcnt(32)
	v_pk_add_f32 v[76:77], v[76:77], v[200:201]
	v_pk_add_f32 v[78:79], v[78:79], v[202:203]
	global_store_dwordx4 v59, v[76:79], s[10:11]
	v_pk_mul_f32 v[224:225], v[240:241], v[76:77]
	v_pk_mul_f32 v[226:227], v[242:243], v[78:79]
	v_cvt_pk_bf16_f32 v4, v224, v225
	v_cvt_pk_bf16_f32 v5, v226, v227
	v_pk_mul_f32 v[230:231], v[76:77], v[76:77]
	v_pk_mul_f32 v[232:233], v[78:79], v[78:79]
	v_add_f32_e32 v230, v230, v231
	v_add_f32_e32 v230, v232, v230
	v_add_f32_e32 v14, v233, v230
	s_waitcnt vmcnt(32)
	v_pk_add_f32 v[92:93], v[92:93], v[204:205]
	v_pk_add_f32 v[94:95], v[94:95], v[206:207]
	global_store_dwordx4 v59, v[92:95], s[10:11] offset:64
	v_pk_mul_f32 v[224:225], v[244:245], v[92:93]
	v_pk_mul_f32 v[226:227], v[246:247], v[94:95]
	v_cvt_pk_bf16_f32 v6, v224, v225
	v_cvt_pk_bf16_f32 v7, v226, v227
	s_nop 1
	v_permlane16_swap_b32 v4, v6
	v_permlane16_swap_b32 v5, v7
	global_store_dwordx4 v63, v[4:7], s[28:29]
	v_pk_mul_f32 v[230:231], v[92:93], v[92:93]
	v_pk_mul_f32 v[232:233], v[94:95], v[94:95]
	v_add_f32_e32 v230, v230, v231
	v_add_f32_e32 v230, v232, v230
	v_add_f32_e32 v230, v233, v230
	v_add_f32_e32 v14, v14, v230
	s_waitcnt vmcnt(33)
	v_pk_add_f32 v[108:109], v[108:109], v[208:209]
	v_pk_add_f32 v[110:111], v[110:111], v[210:211]
	global_store_dwordx4 v59, v[108:111], s[10:11] offset:128
	v_pk_mul_f32 v[224:225], v[248:249], v[108:109]
	v_pk_mul_f32 v[226:227], v[250:251], v[110:111]
	v_cvt_pk_bf16_f32 v4, v224, v225
	v_cvt_pk_bf16_f32 v5, v226, v227
	v_pk_mul_f32 v[230:231], v[108:109], v[108:109]
	v_pk_mul_f32 v[232:233], v[110:111], v[110:111]
	v_add_f32_e32 v230, v230, v231
	v_add_f32_e32 v230, v232, v230
	v_add_f32_e32 v230, v233, v230
	v_add_f32_e32 v14, v14, v230
	s_waitcnt vmcnt(33)
	v_pk_add_f32 v[124:125], v[124:125], v[212:213]
	v_pk_add_f32 v[126:127], v[126:127], v[214:215]
	global_store_dwordx4 v59, v[124:127], s[10:11] offset:192
	v_pk_mul_f32 v[224:225], v[252:253], v[124:125]
	v_pk_mul_f32 v[226:227], v[254:255], v[126:127]
	v_cvt_pk_bf16_f32 v6, v224, v225
	v_cvt_pk_bf16_f32 v7, v226, v227
	s_nop 1
	v_permlane16_swap_b32 v4, v6
	v_permlane16_swap_b32 v5, v7
	global_store_dwordx4 v63, v[4:7], s[28:29] offset:64
	v_pk_mul_f32 v[230:231], v[124:125], v[124:125]
	v_pk_mul_f32 v[232:233], v[126:127], v[126:127]
	v_add_f32_e32 v230, v230, v231
	v_add_f32_e32 v230, v232, v230
	v_add_f32_e32 v15, v233, v230
	s_waitcnt vmcnt(34)
	v_pk_add_f32 v[140:141], v[140:141], v[216:217]
	v_pk_add_f32 v[142:143], v[142:143], v[218:219]
	global_store_dwordx4 v59, v[140:143], s[10:11] offset:256
	v_pk_mul_f32 v[224:225], v[48:49], v[140:141]
	v_pk_mul_f32 v[226:227], v[50:51], v[142:143]
	v_cvt_pk_bf16_f32 v4, v224, v225
	v_cvt_pk_bf16_f32 v5, v226, v227
	v_pk_mul_f32 v[230:231], v[140:141], v[140:141]
	v_pk_mul_f32 v[232:233], v[142:143], v[142:143]
	v_add_f32_e32 v230, v230, v231
	v_add_f32_e32 v230, v232, v230
	v_add_f32_e32 v230, v233, v230
	v_add_f32_e32 v15, v15, v230
	s_waitcnt vmcnt(34)
	v_pk_add_f32 v[156:157], v[156:157], v[220:221]
	v_pk_add_f32 v[158:159], v[158:159], v[222:223]
	global_store_dwordx4 v59, v[156:159], s[10:11] offset:320
	v_pk_mul_f32 v[224:225], v[52:53], v[156:157]
	v_pk_mul_f32 v[226:227], v[54:55], v[158:159]
	v_cvt_pk_bf16_f32 v6, v224, v225
	v_cvt_pk_bf16_f32 v7, v226, v227
	s_nop 1
	v_permlane16_swap_b32 v4, v6
	v_permlane16_swap_b32 v5, v7
	global_store_dwordx4 v63, v[4:7], s[28:29] offset:128
	v_pk_mul_f32 v[230:231], v[156:157], v[156:157]
	v_pk_mul_f32 v[232:233], v[158:159], v[158:159]
	v_add_f32_e32 v230, v230, v231
	v_add_f32_e32 v230, v232, v230
	v_add_f32_e32 v230, v233, v230
	v_add_f32_e32 v15, v15, v230
	v_mov_b32_e32 v224, v234
	v_mov_b32_e32 v225, v235
	v_mov_b32_e32 v226, v236
	v_mov_b32_e32 v227, v237
	v_mov_b32_e32 v228, v238
	v_mov_b32_e32 v229, v239
	v_mov_b32_e32 v230, v14
	v_mov_b32_e32 v231, v15
	v_permlane16_swap_b32 v234, v224
	v_permlane16_swap_b32 v235, v225
	v_permlane16_swap_b32 v236, v226
	v_permlane16_swap_b32 v237, v227
	v_permlane16_swap_b32 v238, v228
	v_permlane16_swap_b32 v239, v229
	v_permlane16_swap_b32 v14, v230
	v_permlane16_swap_b32 v15, v231
	v_add_f32_e32 v234, v234, v224
	v_add_f32_e32 v235, v235, v225
	v_add_f32_e32 v236, v236, v226
	v_add_f32_e32 v237, v237, v227
	v_add_f32_e32 v238, v238, v228
	v_add_f32_e32 v239, v239, v229
	v_add_f32_e32 v14, v14, v230
	v_add_f32_e32 v15, v15, v231
	v_mov_b32_e32 v224, v234
	v_mov_b32_e32 v225, v235
	v_mov_b32_e32 v226, v236
	v_mov_b32_e32 v227, v237
	v_mov_b32_e32 v228, v238
	v_mov_b32_e32 v229, v239
	v_mov_b32_e32 v230, v14
	v_mov_b32_e32 v231, v15
	v_permlane32_swap_b32 v234, v224
	v_permlane32_swap_b32 v235, v225
	v_permlane32_swap_b32 v236, v226
	v_permlane32_swap_b32 v237, v227
	v_permlane32_swap_b32 v238, v228
	v_permlane32_swap_b32 v239, v229
	v_permlane32_swap_b32 v14, v230
	v_permlane32_swap_b32 v15, v231
	v_add_f32_e32 v234, v234, v224
	v_add_f32_e32 v235, v235, v225
	v_add_f32_e32 v236, v236, v226
	v_add_f32_e32 v237, v237, v227
	v_add_f32_e32 v238, v238, v228
	v_add_f32_e32 v239, v239, v229
	v_add_f32_e32 v14, v14, v230
	v_add_f32_e32 v15, v15, v231
	s_and_saveexec_b64 s[2:3], vcc
	global_store_dwordx2 v8, v[234:235], s[26:27]
	global_store_dwordx2 v9, v[236:237], s[26:27]
	global_store_dwordx2 v10, v[238:239], s[26:27]
	global_store_dwordx2 v11, v[14:15], s[26:27]
	s_or_b64 exec, exec, s[2:3]
